# baseline (speedup 1.0000x reference)
.LBB3_2:
	s_load_dword s0, s[0:1], 0x20
	s_and_b32 s14, s2, 7
	v_cvt_f32_ubyte0_e32 v3, s14
	v_lshlrev_b32_e32 v100, 4, v0
	s_mov_b64 s[18:19], 0x20080
	s_waitcnt lgkmcnt(0)
	s_ashr_i32 s1, s0, 31
	s_lshr_b32 s1, s1, 22
	s_add_i32 s1, s0, s1
	s_ashr_i32 s3, s1, 10
	v_cvt_f32_i32_e32 v1, s3
	s_ashr_i32 s1, s1, 31
	s_or_b32 s1, s1, 1
	s_movk_i32 s17, 0x70
	v_rcp_iflag_f32_e32 v2, v1
	s_nop 0
	v_mul_f32_e32 v2, v3, v2
	v_trunc_f32_e32 v2, v2
	v_fma_f32 v3, -v2, v1, v3
	v_cvt_i32_f32_e32 v2, v2
	v_cmp_ge_f32_e64 s[12:13], |v3|, |v1|
	s_and_b64 s[12:13], s[12:13], exec
	s_cselect_b32 s1, s1, 0
	v_readfirstlane_b32 s13, v2
	s_add_i32 s1, s13, s1
	s_lshl_b32 s12, s2, 4
	s_bfe_i32 s13, s1, 0x160000
	s_mul_i32 s1, s1, s3
	s_and_b32 s12, s12, 0x180
	s_sub_i32 s3, s14, s1
	s_lshl_b32 s1, s13, 9
	s_or_b32 s1, s1, s12
	s_lshl_b32 s2, s2, 2
	v_lshrrev_b32_e32 v1, 3, v0
	v_lshrrev_b32_e32 v2, 4, v0
	s_lshl_b32 s3, s3, 10
	s_and_b32 s2, s2, 0xffffff80
	v_xor_b32_e32 v10, v2, v0
	v_or_b32_e32 v2, s1, v1
	s_add_i32 s2, s3, s2
	v_ashrrev_i32_e32 v3, 31, v2
	v_lshlrev_b64 v[4:5], 11, v[2:3]
	v_or_b32_e32 v2, s2, v1
	v_mov_b32_e32 v3, 0
	v_lshlrev_b32_e32 v1, 4, v10
	v_lshlrev_b64 v[6:7], 11, v[2:3]
	v_and_b32_e32 v2, 0x70, v1
	v_add_u32_e32 v1, 0, v100
	v_lshl_add_u64 v[8:9], s[6:7], 0, v[6:7]
	v_lshl_add_u64 v[4:5], s[4:5], 0, v[4:5]
	v_readfirstlane_b32 s6, v1
	v_add_u32_e32 v10, 0x2000, v1
	v_lshl_add_u64 v[6:7], v[4:5], 0, v[2:3]
	v_lshl_add_u64 v[4:5], v[8:9], 0, v[2:3]
	v_add_u32_e32 v2, 0x4000, v1
	s_mov_b32 m0, s6
	s_mov_b64 s[12:13], 0x20000
	v_readfirstlane_b32 s3, v10
	global_load_lds_dwordx4 v[6:7], off
	v_lshl_add_u64 v[8:9], v[6:7], 0, s[12:13]
	s_mov_b32 m0, s3
	v_readfirstlane_b32 s4, v2
	v_add_u32_e32 v2, 0x6000, v1
	global_load_lds_dwordx4 v[8:9], off
	s_mov_b32 m0, s4
	v_readfirstlane_b32 s5, v2
	v_add_u32_e32 v12, 0x8000, v1
	global_load_lds_dwordx4 v[4:5], off
	v_lshl_add_u64 v[8:9], v[4:5], 0, s[12:13]
	s_mov_b32 m0, s5
	s_mov_b64 s[12:13], 0x80
	v_readfirstlane_b32 s16, v12
	v_add_u32_e32 v12, 0xa000, v1
	global_load_lds_dwordx4 v[8:9], off
	v_lshl_add_u64 v[8:9], v[4:5], 0, s[12:13]
	v_add_u32_e32 v2, 0xc000, v1
	v_lshl_add_u64 v[10:11], v[6:7], 0, s[12:13]
	s_mov_b32 m0, s16
	v_readfirstlane_b32 s13, v12
	global_load_lds_dwordx4 v[10:11], off
	v_lshl_add_u64 v[10:11], v[6:7], 0, s[18:19]
	s_mov_b32 m0, s13
	v_readfirstlane_b32 s14, v2
	v_add_u32_e32 v2, 0xe000, v1
	global_load_lds_dwordx4 v[10:11], off
	s_mov_b32 m0, s14
	v_readfirstlane_b32 s15, v2
	s_add_i32 s7, 0, 0x14000
	v_add_u32_e32 v12, 0x10000, v1
	global_load_lds_dwordx4 v[8:9], off
	v_lshl_add_u64 v[8:9], v[4:5], 0, s[18:19]
	s_mov_b32 m0, s15
	s_mov_b64 s[18:19], 0x100
	v_add_u32_e32 v2, s7, v100
	v_readfirstlane_b32 s7, v12
	v_add_u32_e32 v1, 0x12000, v1
	global_load_lds_dwordx4 v[8:9], off
	v_lshl_add_u64 v[8:9], v[4:5], 0, s[18:19]
	v_lshl_add_u64 v[10:11], v[6:7], 0, s[18:19]
	s_mov_b32 m0, s7
	s_mov_b64 s[18:19], 0x20100
	v_readfirstlane_b32 s7, v1
	global_load_lds_dwordx4 v[10:11], off
	v_lshl_add_u64 v[10:11], v[6:7], 0, s[18:19]
	s_mov_b32 m0, s7
	v_readfirstlane_b32 s7, v2
	v_add_u32_e32 v1, 0x2000, v2
	global_load_lds_dwordx4 v[10:11], off
	s_mov_b32 m0, s7
	v_readfirstlane_b32 s12, v1
	global_load_lds_dwordx4 v[8:9], off
	v_lshl_add_u64 v[8:9], v[4:5], 0, s[18:19]
	s_mov_b32 m0, s12
	v_lshrrev_b32_e32 v1, 2, v0
	global_load_lds_dwordx4 v[8:9], off
	v_and_b32_e32 v8, 15, v0
	v_and_b32_e32 v1, 0x60, v1
	v_or_b32_e32 v10, v1, v8
	v_lshlrev_b32_e32 v101, 7, v10
	v_lshlrev_b32_e32 v10, 7, v0
	v_and_b32_e32 v2, 63, v0
	v_lshlrev_b32_e32 v9, 3, v0
	v_and_b32_e32 v102, 0x2780, v10
	v_bitop3_b32 v10, v2, s17, v9 bitop3:0x48
	v_add_u32_e32 v56, 0, v102
	v_add_u32_e32 v48, 0, v101
	s_waitcnt vmcnt(8) lgkmcnt(0)
	s_barrier
	v_add_u32_e32 v2, v56, v10
	v_add_u32_e32 v11, v48, v10
	v_bitop3_b32 v9, v0, v9, 63 bitop3:0x6c
	v_mov_b32_e32 v10, 0x70
	ds_read_b128 v[12:15], v2 offset:16384
	ds_read_b128 v[16:19], v2 offset:18432
	ds_read_b128 v[20:23], v11
	ds_read_b128 v[24:27], v11 offset:2048
	ds_read_b128 v[32:35], v2 offset:20480
	ds_read_b128 v[40:43], v2 offset:22528
	v_bitop3_b32 v103, v9, 64, v10 bitop3:0x6c
	v_add_u32_e32 v10, v48, v103
	v_add_u32_e32 v9, v56, v103
	s_waitcnt lgkmcnt(0)
	v_mfma_f32_16x16x32_f16 v[28:31], v[12:15], v[20:23], 0
	ds_read_b128 v[48:51], v10
	ds_read_b128 v[52:55], v10 offset:2048
	v_mfma_f32_16x16x32_f16 v[36:39], v[16:19], v[20:23], 0
	v_mfma_f32_16x16x32_f16 v[44:47], v[32:35], v[20:23], 0
	ds_read_b128 v[56:59], v9 offset:16384
	ds_read_b128 v[60:63], v9 offset:18432
	v_mfma_f32_16x16x32_f16 v[20:23], v[40:43], v[20:23], 0
	v_mfma_f32_16x16x32_f16 v[12:15], v[12:15], v[24:27], 0
	ds_read_b128 v[64:67], v9 offset:20480
	ds_read_b128 v[68:71], v9 offset:22528
	v_mfma_f32_16x16x32_f16 v[16:19], v[16:19], v[24:27], 0
	v_mfma_f32_16x16x32_f16 v[32:35], v[32:35], v[24:27], 0
	v_mfma_f32_16x16x32_f16 v[24:27], v[40:43], v[24:27], 0
	s_mov_b64 s[18:19], 0x180
	s_mov_b32 m0, s6
	s_waitcnt vmcnt(4) lgkmcnt(0)
	s_barrier
	v_lshl_add_u64 v[40:41], v[4:5], 0, s[18:19]
	v_lshl_add_u64 v[42:43], v[6:7], 0, s[18:19]
	s_mov_b64 s[18:19], 0x20180
	global_load_lds_dwordx4 v[42:43], off
	v_lshl_add_u64 v[42:43], v[6:7], 0, s[18:19]
	s_mov_b32 m0, s3
	s_nop 0
	global_load_lds_dwordx4 v[42:43], off
	s_mov_b32 m0, s4
	s_nop 0
	global_load_lds_dwordx4 v[40:41], off
	v_lshl_add_u64 v[40:41], v[4:5], 0, s[18:19]
	s_mov_b32 m0, s5
	s_nop 0
	global_load_lds_dwordx4 v[40:41], off
	ds_read_b128 v[40:43], v11 offset:32768
	ds_read_b128 v[72:75], v11 offset:34816
	ds_read_b128 v[76:79], v2 offset:49152
	ds_read_b128 v[80:83], v2 offset:51200
	ds_read_b128 v[84:87], v2 offset:53248
	ds_read_b128 v[88:91], v2 offset:55296
	v_mfma_f32_16x16x32_f16 v[28:31], v[56:59], v[48:51], v[28:31]
	v_mfma_f32_16x16x32_f16 v[36:39], v[60:63], v[48:51], v[36:39]
	v_mfma_f32_16x16x32_f16 v[44:47], v[64:67], v[48:51], v[44:47]
	v_mfma_f32_16x16x32_f16 v[20:23], v[68:71], v[48:51], v[20:23]
	v_mfma_f32_16x16x32_f16 v[12:15], v[56:59], v[52:55], v[12:15]
	v_mfma_f32_16x16x32_f16 v[16:19], v[60:63], v[52:55], v[16:19]
	v_mfma_f32_16x16x32_f16 v[32:35], v[64:67], v[52:55], v[32:35]
	v_mfma_f32_16x16x32_f16 v[24:27], v[68:71], v[52:55], v[24:27]
	s_waitcnt lgkmcnt(0)
	v_mfma_f32_16x16x32_f16 v[28:31], v[76:79], v[40:43], v[28:31]
	ds_read_b128 v[52:55], v10 offset:32768
	ds_read_b128 v[56:59], v10 offset:34816
	v_mfma_f32_16x16x32_f16 v[36:39], v[80:83], v[40:43], v[36:39]
	v_mfma_f32_16x16x32_f16 v[44:47], v[84:87], v[40:43], v[44:47]
	v_mfma_f32_16x16x32_f16 v[20:23], v[88:91], v[40:43], v[20:23]
	v_mfma_f32_16x16x32_f16 v[40:43], v[76:79], v[72:75], v[12:15]
	ds_read_b128 v[60:63], v9 offset:49152
	ds_read_b128 v[64:67], v9 offset:51200
	ds_read_b128 v[68:71], v9 offset:53248
	ds_read_b128 v[76:79], v9 offset:55296
	v_mfma_f32_16x16x32_f16 v[48:51], v[80:83], v[72:75], v[16:19]
	v_mfma_f32_16x16x32_f16 v[32:35], v[84:87], v[72:75], v[32:35]
	v_mfma_f32_16x16x32_f16 v[24:27], v[88:91], v[72:75], v[24:27]
	s_mov_b64 s[18:19], 0x200
	s_mov_b32 m0, s16
	s_waitcnt vmcnt(4) lgkmcnt(0)
	s_barrier
	v_lshl_add_u64 v[12:13], v[4:5], 0, s[18:19]
	v_lshl_add_u64 v[14:15], v[6:7], 0, s[18:19]
	s_mov_b64 s[18:19], 0x20200
	global_load_lds_dwordx4 v[14:15], off
	v_lshl_add_u64 v[14:15], v[6:7], 0, s[18:19]
	s_mov_b32 m0, s13
	v_add_u32_e32 v16, 0x15000, v2
	global_load_lds_dwordx4 v[14:15], off
	s_mov_b32 m0, s14
	v_add_u32_e32 v14, 0x14000, v2
	global_load_lds_dwordx4 v[12:13], off
	v_lshl_add_u64 v[12:13], v[4:5], 0, s[18:19]
	s_mov_b32 m0, s15
	v_add_u32_e32 v15, 0x14800, v2
	global_load_lds_dwordx4 v[12:13], off
	v_add_u32_e32 v12, 0x10000, v11
	v_add_u32_e32 v13, 0x10800, v11
	ds_read_b128 v[72:75], v12
	ds_read_b128 v[80:83], v13
	ds_read_b128 v[84:87], v14
	ds_read_b128 v[88:91], v15
	v_add_u32_e32 v17, 0x15800, v2
	ds_read_b128 v[92:95], v16
	ds_read_b128 v[96:99], v17
	v_mfma_f32_16x16x32_f16 v[28:31], v[60:63], v[52:55], v[28:31]
	v_mfma_f32_16x16x32_f16 v[36:39], v[64:67], v[52:55], v[36:39]
	v_mfma_f32_16x16x32_f16 v[44:47], v[68:71], v[52:55], v[44:47]
	v_mfma_f32_16x16x32_f16 v[18:21], v[76:79], v[52:55], v[20:23]
	v_mfma_f32_16x16x32_f16 v[40:43], v[60:63], v[56:59], v[40:43]
	v_mfma_f32_16x16x32_f16 v[48:51], v[64:67], v[56:59], v[48:51]
	v_mfma_f32_16x16x32_f16 v[32:35], v[68:71], v[56:59], v[32:35]
	v_mfma_f32_16x16x32_f16 v[22:25], v[76:79], v[56:59], v[24:27]
	s_add_i32 s17, 0, 0x10000
	s_waitcnt lgkmcnt(0)
	v_mfma_f32_16x16x32_f16 v[52:55], v[96:99], v[72:75], v[18:21]
	s_nop 2
	v_add_u32_e32 v18, s17, v103
	v_add_u32_e32 v19, v18, v101
	v_add_u32_e32 v18, v18, v102
	v_mfma_f32_16x16x32_f16 v[26:29], v[84:87], v[72:75], v[28:31]
	ds_read_b128 v[56:59], v19
	ds_read_b128 v[60:63], v19 offset:2048
	v_mfma_f32_16x16x32_f16 v[36:39], v[88:91], v[72:75], v[36:39]
	v_mfma_f32_16x16x32_f16 v[44:47], v[92:95], v[72:75], v[44:47]
	ds_read_b128 v[64:67], v18 offset:16384
	ds_read_b128 v[68:71], v18 offset:18432
	ds_read_b128 v[72:75], v18 offset:20480
	ds_read_b128 v[76:79], v18 offset:22528
	v_mfma_f32_16x16x32_f16 v[40:43], v[84:87], v[80:83], v[40:43]
	v_mfma_f32_16x16x32_f16 v[48:51], v[88:91], v[80:83], v[48:51]
	v_mfma_f32_16x16x32_f16 v[30:33], v[92:95], v[80:83], v[32:35]
	v_mfma_f32_16x16x32_f16 v[20:23], v[96:99], v[80:83], v[22:25]
	s_mov_b64 s[18:19], 0x280
	v_add_u32_e32 v80, s17, v100
	s_nop 0
	v_lshl_add_u64 v[24:25], v[4:5], 0, s[18:19]
	v_lshl_add_u64 v[34:35], v[6:7], 0, s[18:19]
	v_readfirstlane_b32 s18, v80
	v_add_u32_e32 v80, 0x2000, v80
	s_waitcnt vmcnt(4) lgkmcnt(0)
	s_barrier
	s_mov_b32 m0, s18
	s_mov_b64 s[20:21], 0x20280
	v_readfirstlane_b32 s17, v80
	global_load_lds_dwordx4 v[34:35], off
	v_lshl_add_u64 v[34:35], v[6:7], 0, s[20:21]
	s_mov_b32 m0, s17
	s_nop 0
	global_load_lds_dwordx4 v[34:35], off
	s_mov_b32 m0, s7
	s_nop 0
	global_load_lds_dwordx4 v[24:25], off
	v_lshl_add_u64 v[24:25], v[4:5], 0, s[20:21]
	s_mov_b32 m0, s12
	s_nop 0
	global_load_lds_dwordx4 v[24:25], off
	ds_read_b128 v[80:83], v11
	ds_read_b128 v[84:87], v11 offset:2048
	ds_read_b128 v[88:91], v2 offset:16384
	ds_read_b128 v[92:95], v2 offset:18432
	ds_read_b128 v[96:99], v2 offset:20480
	ds_read_b128 v[100:103], v2 offset:22528
	v_mfma_f32_16x16x32_f16 v[24:27], v[64:67], v[56:59], v[26:29]
	v_mfma_f32_16x16x32_f16 v[34:37], v[68:71], v[56:59], v[36:39]
	v_mfma_f32_16x16x32_f16 v[44:47], v[72:75], v[56:59], v[44:47]
	v_mfma_f32_16x16x32_f16 v[52:55], v[76:79], v[56:59], v[52:55]
	v_mfma_f32_16x16x32_f16 v[38:41], v[64:67], v[60:63], v[40:43]
	v_mfma_f32_16x16x32_f16 v[48:51], v[68:71], v[60:63], v[48:51]
	v_mfma_f32_16x16x32_f16 v[28:31], v[72:75], v[60:63], v[30:33]
	v_mfma_f32_16x16x32_f16 v[20:23], v[76:79], v[60:63], v[20:23]
	s_waitcnt lgkmcnt(0)
	v_mfma_f32_16x16x32_f16 v[24:27], v[88:91], v[80:83], v[24:27]
	ds_read_b128 v[56:59], v10
	ds_read_b128 v[60:63], v10 offset:2048
	v_mfma_f32_16x16x32_f16 v[32:35], v[92:95], v[80:83], v[34:37]
	v_mfma_f32_16x16x32_f16 v[42:45], v[96:99], v[80:83], v[44:47]
	ds_read_b128 v[64:67], v9 offset:16384
	ds_read_b128 v[68:71], v9 offset:18432
	v_mfma_f32_16x16x32_f16 v[52:55], v[100:103], v[80:83], v[52:55]
	v_mfma_f32_16x16x32_f16 v[36:39], v[88:91], v[84:87], v[38:41]
	ds_read_b128 v[72:75], v9 offset:20480
	ds_read_b128 v[76:79], v9 offset:22528
	v_mfma_f32_16x16x32_f16 v[46:49], v[92:95], v[84:87], v[48:51]
	v_mfma_f32_16x16x32_f16 v[28:31], v[96:99], v[84:87], v[28:31]
	v_mfma_f32_16x16x32_f16 v[20:23], v[100:103], v[84:87], v[20:23]
	s_mov_b64 s[20:21], 0x300
	s_mov_b32 m0, s6
	s_waitcnt vmcnt(4) lgkmcnt(0)
	s_barrier
	v_lshl_add_u64 v[40:41], v[4:5], 0, s[20:21]
	v_lshl_add_u64 v[50:51], v[6:7], 0, s[20:21]
	s_mov_b64 s[20:21], 0x20300
	global_load_lds_dwordx4 v[50:51], off
	v_lshl_add_u64 v[50:51], v[6:7], 0, s[20:21]
	s_mov_b32 m0, s3
	s_nop 0
	global_load_lds_dwordx4 v[50:51], off
	s_mov_b32 m0, s4
	s_nop 0
	global_load_lds_dwordx4 v[40:41], off
	v_lshl_add_u64 v[40:41], v[4:5], 0, s[20:21]
	s_mov_b32 m0, s5
	s_nop 0
	global_load_lds_dwordx4 v[40:41], off
	ds_read_b128 v[80:83], v11 offset:32768
	ds_read_b128 v[84:87], v11 offset:34816
	ds_read_b128 v[88:91], v2 offset:49152
	ds_read_b128 v[92:95], v2 offset:51200
	ds_read_b128 v[96:99], v2 offset:53248
	ds_read_b128 v[100:103], v2 offset:55296
	v_mfma_f32_16x16x32_f16 v[24:27], v[64:67], v[56:59], v[24:27]
	v_mfma_f32_16x16x32_f16 v[32:35], v[68:71], v[56:59], v[32:35]
	v_mfma_f32_16x16x32_f16 v[40:43], v[72:75], v[56:59], v[42:45]
	v_mfma_f32_16x16x32_f16 v[50:53], v[76:79], v[56:59], v[52:55]
	v_mfma_f32_16x16x32_f16 v[36:39], v[64:67], v[60:63], v[36:39]
	v_mfma_f32_16x16x32_f16 v[44:47], v[68:71], v[60:63], v[46:49]
	v_mfma_f32_16x16x32_f16 v[28:31], v[72:75], v[60:63], v[28:31]
	v_mfma_f32_16x16x32_f16 v[20:23], v[76:79], v[60:63], v[20:23]
	s_waitcnt lgkmcnt(0)
	v_mfma_f32_16x16x32_f16 v[48:51], v[100:103], v[80:83], v[50:53]
	s_nop 2
	ds_read_b128 v[52:55], v10 offset:32768
	ds_read_b128 v[56:59], v10 offset:34816
	ds_read_b128 v[60:63], v9 offset:49152
	ds_read_b128 v[64:67], v9 offset:51200
	ds_read_b128 v[68:71], v9 offset:53248
	ds_read_b128 v[72:75], v9 offset:55296
	v_mfma_f32_16x16x32_f16 v[24:27], v[88:91], v[80:83], v[24:27]
	v_mfma_f32_16x16x32_f16 v[32:35], v[92:95], v[80:83], v[32:35]
	v_mfma_f32_16x16x32_f16 v[40:43], v[96:99], v[80:83], v[40:43]
	v_mfma_f32_16x16x32_f16 v[36:39], v[88:91], v[84:87], v[36:39]
	v_mfma_f32_16x16x32_f16 v[44:47], v[92:95], v[84:87], v[44:47]
	v_mfma_f32_16x16x32_f16 v[28:31], v[96:99], v[84:87], v[28:31]
	v_mfma_f32_16x16x32_f16 v[20:23], v[100:103], v[84:87], v[20:23]
	s_mov_b64 s[20:21], 0x380
	s_mov_b32 m0, s16
	s_waitcnt vmcnt(4) lgkmcnt(0)
	s_barrier
	v_lshl_add_u64 v[76:77], v[4:5], 0, s[20:21]
	v_lshl_add_u64 v[78:79], v[6:7], 0, s[20:21]
	s_mov_b64 s[20:21], 0x20380
	global_load_lds_dwordx4 v[78:79], off
	v_lshl_add_u64 v[78:79], v[6:7], 0, s[20:21]
	s_mov_b32 m0, s13
	s_nop 0
	global_load_lds_dwordx4 v[78:79], off
	s_mov_b32 m0, s14
	s_nop 0
	global_load_lds_dwordx4 v[76:77], off
	v_lshl_add_u64 v[76:77], v[4:5], 0, s[20:21]
	s_mov_b32 m0, s15
	s_nop 0
	global_load_lds_dwordx4 v[76:77], off
	ds_read_b128 v[76:79], v12
	ds_read_b128 v[80:83], v13
	ds_read_b128 v[84:87], v14
	ds_read_b128 v[88:91], v15
	ds_read_b128 v[92:95], v16
	ds_read_b128 v[96:99], v17
	v_mfma_f32_16x16x32_f16 v[24:27], v[60:63], v[52:55], v[24:27]
	v_mfma_f32_16x16x32_f16 v[32:35], v[64:67], v[52:55], v[32:35]
	v_mfma_f32_16x16x32_f16 v[40:43], v[68:71], v[52:55], v[40:43]
	v_mfma_f32_16x16x32_f16 v[48:51], v[72:75], v[52:55], v[48:51]
	v_mfma_f32_16x16x32_f16 v[36:39], v[60:63], v[56:59], v[36:39]
	v_mfma_f32_16x16x32_f16 v[44:47], v[64:67], v[56:59], v[44:47]
	v_mfma_f32_16x16x32_f16 v[28:31], v[68:71], v[56:59], v[28:31]
	v_mfma_f32_16x16x32_f16 v[20:23], v[72:75], v[56:59], v[20:23]
	s_waitcnt lgkmcnt(0)
	v_mfma_f32_16x16x32_f16 v[24:27], v[84:87], v[76:79], v[24:27]
	ds_read_b128 v[52:55], v19
	ds_read_b128 v[56:59], v19 offset:2048
	v_mfma_f32_16x16x32_f16 v[32:35], v[88:91], v[76:79], v[32:35]
	v_mfma_f32_16x16x32_f16 v[40:43], v[92:95], v[76:79], v[40:43]
	ds_read_b128 v[60:63], v18 offset:16384
	ds_read_b128 v[64:67], v18 offset:18432
	v_mfma_f32_16x16x32_f16 v[48:51], v[96:99], v[76:79], v[48:51]
	v_mfma_f32_16x16x32_f16 v[36:39], v[84:87], v[80:83], v[36:39]
	ds_read_b128 v[68:71], v18 offset:20480
	ds_read_b128 v[72:75], v18 offset:22528
	v_mfma_f32_16x16x32_f16 v[44:47], v[88:91], v[80:83], v[44:47]
	v_mfma_f32_16x16x32_f16 v[28:31], v[92:95], v[80:83], v[28:31]
	v_mfma_f32_16x16x32_f16 v[20:23], v[96:99], v[80:83], v[20:23]
	s_mov_b64 s[20:21], 0x400
	s_mov_b32 m0, s18
	s_waitcnt vmcnt(4) lgkmcnt(0)
	s_barrier
	v_lshl_add_u64 v[76:77], v[4:5], 0, s[20:21]
	v_lshl_add_u64 v[78:79], v[6:7], 0, s[20:21]
	s_mov_b64 s[20:21], 0x20400
	global_load_lds_dwordx4 v[78:79], off
	v_lshl_add_u64 v[78:79], v[6:7], 0, s[20:21]
	s_mov_b32 m0, s17
	s_nop 0
	global_load_lds_dwordx4 v[78:79], off
	s_mov_b32 m0, s7
	s_nop 0
	global_load_lds_dwordx4 v[76:77], off
	v_lshl_add_u64 v[76:77], v[4:5], 0, s[20:21]
	s_mov_b32 m0, s12
	s_nop 0
	global_load_lds_dwordx4 v[76:77], off
	ds_read_b128 v[76:79], v11
	ds_read_b128 v[80:83], v11 offset:2048
	ds_read_b128 v[84:87], v2 offset:16384
	ds_read_b128 v[88:91], v2 offset:18432
	ds_read_b128 v[92:95], v2 offset:20480
	ds_read_b128 v[96:99], v2 offset:22528
	v_mfma_f32_16x16x32_f16 v[24:27], v[60:63], v[52:55], v[24:27]
	v_mfma_f32_16x16x32_f16 v[32:35], v[64:67], v[52:55], v[32:35]
	v_mfma_f32_16x16x32_f16 v[40:43], v[68:71], v[52:55], v[40:43]
	v_mfma_f32_16x16x32_f16 v[48:51], v[72:75], v[52:55], v[48:51]
	v_mfma_f32_16x16x32_f16 v[36:39], v[60:63], v[56:59], v[36:39]
	v_mfma_f32_16x16x32_f16 v[44:47], v[64:67], v[56:59], v[44:47]
	v_mfma_f32_16x16x32_f16 v[28:31], v[68:71], v[56:59], v[28:31]
	v_mfma_f32_16x16x32_f16 v[20:23], v[72:75], v[56:59], v[20:23]
	s_waitcnt lgkmcnt(0)
	v_mfma_f32_16x16x32_f16 v[24:27], v[84:87], v[76:79], v[24:27]
	ds_read_b128 v[52:55], v10
	ds_read_b128 v[56:59], v10 offset:2048
	v_mfma_f32_16x16x32_f16 v[32:35], v[88:91], v[76:79], v[32:35]
	v_mfma_f32_16x16x32_f16 v[40:43], v[92:95], v[76:79], v[40:43]
	ds_read_b128 v[60:63], v9 offset:16384
	ds_read_b128 v[64:67], v9 offset:18432
	v_mfma_f32_16x16x32_f16 v[48:51], v[96:99], v[76:79], v[48:51]
	v_mfma_f32_16x16x32_f16 v[36:39], v[84:87], v[80:83], v[36:39]
	ds_read_b128 v[68:71], v9 offset:20480
	ds_read_b128 v[72:75], v9 offset:22528
	v_mfma_f32_16x16x32_f16 v[44:47], v[88:91], v[80:83], v[44:47]
	v_mfma_f32_16x16x32_f16 v[28:31], v[92:95], v[80:83], v[28:31]
	v_mfma_f32_16x16x32_f16 v[20:23], v[96:99], v[80:83], v[20:23]
	s_mov_b64 s[20:21], 0x480
	s_mov_b32 m0, s6
	s_waitcnt vmcnt(4) lgkmcnt(0)
	s_barrier
	v_lshl_add_u64 v[76:77], v[4:5], 0, s[20:21]
	v_lshl_add_u64 v[78:79], v[6:7], 0, s[20:21]
	s_mov_b64 s[20:21], 0x20480
	global_load_lds_dwordx4 v[78:79], off
	v_lshl_add_u64 v[78:79], v[6:7], 0, s[20:21]
	s_mov_b32 m0, s3
	s_nop 0
	global_load_lds_dwordx4 v[78:79], off
	s_mov_b32 m0, s4
	s_nop 0
	global_load_lds_dwordx4 v[76:77], off
	v_lshl_add_u64 v[76:77], v[4:5], 0, s[20:21]
	s_mov_b32 m0, s5
	s_nop 0
	global_load_lds_dwordx4 v[76:77], off
	ds_read_b128 v[76:79], v11 offset:32768
	ds_read_b128 v[80:83], v11 offset:34816
	ds_read_b128 v[84:87], v2 offset:49152
	ds_read_b128 v[88:91], v2 offset:51200
	ds_read_b128 v[92:95], v2 offset:53248
	ds_read_b128 v[96:99], v2 offset:55296
	v_mfma_f32_16x16x32_f16 v[24:27], v[60:63], v[52:55], v[24:27]
	v_mfma_f32_16x16x32_f16 v[32:35], v[64:67], v[52:55], v[32:35]
	v_mfma_f32_16x16x32_f16 v[40:43], v[68:71], v[52:55], v[40:43]
	v_mfma_f32_16x16x32_f16 v[48:51], v[72:75], v[52:55], v[48:51]
	v_mfma_f32_16x16x32_f16 v[36:39], v[60:63], v[56:59], v[36:39]
	v_mfma_f32_16x16x32_f16 v[44:47], v[64:67], v[56:59], v[44:47]
	v_mfma_f32_16x16x32_f16 v[28:31], v[68:71], v[56:59], v[28:31]
	v_mfma_f32_16x16x32_f16 v[20:23], v[72:75], v[56:59], v[20:23]
	s_waitcnt lgkmcnt(0)
	v_mfma_f32_16x16x32_f16 v[24:27], v[84:87], v[76:79], v[24:27]
	ds_read_b128 v[52:55], v10 offset:32768
	ds_read_b128 v[56:59], v10 offset:34816
	v_mfma_f32_16x16x32_f16 v[32:35], v[88:91], v[76:79], v[32:35]
	v_mfma_f32_16x16x32_f16 v[40:43], v[92:95], v[76:79], v[40:43]
	ds_read_b128 v[60:63], v9 offset:49152
	ds_read_b128 v[64:67], v9 offset:51200
	v_mfma_f32_16x16x32_f16 v[48:51], v[96:99], v[76:79], v[48:51]
	v_mfma_f32_16x16x32_f16 v[36:39], v[84:87], v[80:83], v[36:39]
	ds_read_b128 v[68:71], v9 offset:53248
	ds_read_b128 v[72:75], v9 offset:55296
	v_mfma_f32_16x16x32_f16 v[44:47], v[88:91], v[80:83], v[44:47]
	v_mfma_f32_16x16x32_f16 v[28:31], v[92:95], v[80:83], v[28:31]
	v_mfma_f32_16x16x32_f16 v[20:23], v[96:99], v[80:83], v[20:23]
	s_mov_b64 s[20:21], 0x500
	s_mov_b32 m0, s16
	s_waitcnt vmcnt(4) lgkmcnt(0)
	s_barrier
	v_lshl_add_u64 v[76:77], v[4:5], 0, s[20:21]
	v_lshl_add_u64 v[78:79], v[6:7], 0, s[20:21]
	s_mov_b64 s[20:21], 0x20500
	global_load_lds_dwordx4 v[78:79], off
	v_lshl_add_u64 v[78:79], v[6:7], 0, s[20:21]
	s_mov_b32 m0, s13
	s_nop 0
	global_load_lds_dwordx4 v[78:79], off
	s_mov_b32 m0, s14
	s_nop 0
	global_load_lds_dwordx4 v[76:77], off
	v_lshl_add_u64 v[76:77], v[4:5], 0, s[20:21]
	s_mov_b32 m0, s15
	s_nop 0
	global_load_lds_dwordx4 v[76:77], off
	ds_read_b128 v[76:79], v12
	ds_read_b128 v[80:83], v13
	ds_read_b128 v[84:87], v14
	ds_read_b128 v[88:91], v15
	ds_read_b128 v[92:95], v16
	ds_read_b128 v[96:99], v17
	v_mfma_f32_16x16x32_f16 v[24:27], v[60:63], v[52:55], v[24:27]
	v_mfma_f32_16x16x32_f16 v[32:35], v[64:67], v[52:55], v[32:35]
	v_mfma_f32_16x16x32_f16 v[40:43], v[68:71], v[52:55], v[40:43]
	v_mfma_f32_16x16x32_f16 v[48:51], v[72:75], v[52:55], v[48:51]
	v_mfma_f32_16x16x32_f16 v[36:39], v[60:63], v[56:59], v[36:39]
	v_mfma_f32_16x16x32_f16 v[44:47], v[64:67], v[56:59], v[44:47]
	v_mfma_f32_16x16x32_f16 v[28:31], v[68:71], v[56:59], v[28:31]
	v_mfma_f32_16x16x32_f16 v[20:23], v[72:75], v[56:59], v[20:23]
	s_waitcnt lgkmcnt(0)
	v_mfma_f32_16x16x32_f16 v[24:27], v[84:87], v[76:79], v[24:27]
	ds_read_b128 v[52:55], v19
	ds_read_b128 v[56:59], v19 offset:2048
	v_mfma_f32_16x16x32_f16 v[32:35], v[88:91], v[76:79], v[32:35]
	v_mfma_f32_16x16x32_f16 v[40:43], v[92:95], v[76:79], v[40:43]
	ds_read_b128 v[60:63], v18 offset:16384
	ds_read_b128 v[64:67], v18 offset:18432
	v_mfma_f32_16x16x32_f16 v[48:51], v[96:99], v[76:79], v[48:51]
	v_mfma_f32_16x16x32_f16 v[36:39], v[84:87], v[80:83], v[36:39]
	ds_read_b128 v[68:71], v18 offset:20480
	ds_read_b128 v[72:75], v18 offset:22528
	v_mfma_f32_16x16x32_f16 v[44:47], v[88:91], v[80:83], v[44:47]
	v_mfma_f32_16x16x32_f16 v[28:31], v[92:95], v[80:83], v[28:31]
	v_mfma_f32_16x16x32_f16 v[20:23], v[96:99], v[80:83], v[20:23]
	s_mov_b64 s[20:21], 0x580
	s_mov_b32 m0, s18
	s_waitcnt vmcnt(4) lgkmcnt(0)
	s_barrier
	v_lshl_add_u64 v[76:77], v[4:5], 0, s[20:21]
	v_lshl_add_u64 v[78:79], v[6:7], 0, s[20:21]
	s_mov_b64 s[20:21], 0x20580
	global_load_lds_dwordx4 v[78:79], off
	v_lshl_add_u64 v[78:79], v[6:7], 0, s[20:21]
	s_mov_b32 m0, s17
	s_nop 0
	global_load_lds_dwordx4 v[78:79], off
	s_mov_b32 m0, s7
	s_nop 0
	global_load_lds_dwordx4 v[76:77], off
	v_lshl_add_u64 v[76:77], v[4:5], 0, s[20:21]
	s_mov_b32 m0, s12
	s_nop 0
	global_load_lds_dwordx4 v[76:77], off
	ds_read_b128 v[76:79], v11
	ds_read_b128 v[80:83], v11 offset:2048
	ds_read_b128 v[84:87], v2 offset:16384
	ds_read_b128 v[88:91], v2 offset:18432
	ds_read_b128 v[92:95], v2 offset:20480
	ds_read_b128 v[96:99], v2 offset:22528
	v_mfma_f32_16x16x32_f16 v[24:27], v[60:63], v[52:55], v[24:27]
	v_mfma_f32_16x16x32_f16 v[32:35], v[64:67], v[52:55], v[32:35]
	v_mfma_f32_16x16x32_f16 v[40:43], v[68:71], v[52:55], v[40:43]
	v_mfma_f32_16x16x32_f16 v[48:51], v[72:75], v[52:55], v[48:51]
	v_mfma_f32_16x16x32_f16 v[36:39], v[60:63], v[56:59], v[36:39]
	v_mfma_f32_16x16x32_f16 v[44:47], v[64:67], v[56:59], v[44:47]
	v_mfma_f32_16x16x32_f16 v[28:31], v[68:71], v[56:59], v[28:31]
	v_mfma_f32_16x16x32_f16 v[20:23], v[72:75], v[56:59], v[20:23]
	s_waitcnt lgkmcnt(0)
	v_mfma_f32_16x16x32_f16 v[24:27], v[84:87], v[76:79], v[24:27]
	ds_read_b128 v[52:55], v10
	ds_read_b128 v[56:59], v10 offset:2048
	v_mfma_f32_16x16x32_f16 v[32:35], v[88:91], v[76:79], v[32:35]
	v_mfma_f32_16x16x32_f16 v[40:43], v[92:95], v[76:79], v[40:43]
	ds_read_b128 v[60:63], v9 offset:16384
	ds_read_b128 v[64:67], v9 offset:18432
	v_mfma_f32_16x16x32_f16 v[48:51], v[96:99], v[76:79], v[48:51]
	v_mfma_f32_16x16x32_f16 v[36:39], v[84:87], v[80:83], v[36:39]
	ds_read_b128 v[68:71], v9 offset:20480
	ds_read_b128 v[72:75], v9 offset:22528
	v_mfma_f32_16x16x32_f16 v[44:47], v[88:91], v[80:83], v[44:47]
	v_mfma_f32_16x16x32_f16 v[28:31], v[92:95], v[80:83], v[28:31]
	v_mfma_f32_16x16x32_f16 v[20:23], v[96:99], v[80:83], v[20:23]
	s_mov_b64 s[20:21], 0x600
	s_mov_b32 m0, s6
	s_waitcnt vmcnt(4) lgkmcnt(0)
	s_barrier
	v_lshl_add_u64 v[76:77], v[4:5], 0, s[20:21]
	v_lshl_add_u64 v[78:79], v[6:7], 0, s[20:21]
	s_mov_b64 s[20:21], 0x20600
	global_load_lds_dwordx4 v[78:79], off
	v_lshl_add_u64 v[78:79], v[6:7], 0, s[20:21]
	s_mov_b32 m0, s3
	s_nop 0
	global_load_lds_dwordx4 v[78:79], off
	s_mov_b32 m0, s4
	s_nop 0
	global_load_lds_dwordx4 v[76:77], off
	v_lshl_add_u64 v[76:77], v[4:5], 0, s[20:21]
	s_mov_b32 m0, s5
	s_nop 0
	global_load_lds_dwordx4 v[76:77], off
	ds_read_b128 v[76:79], v11 offset:32768
	ds_read_b128 v[80:83], v11 offset:34816
	ds_read_b128 v[84:87], v2 offset:49152
	ds_read_b128 v[88:91], v2 offset:51200
	ds_read_b128 v[92:95], v2 offset:53248
	ds_read_b128 v[96:99], v2 offset:55296
	v_mfma_f32_16x16x32_f16 v[24:27], v[60:63], v[52:55], v[24:27]
	v_mfma_f32_16x16x32_f16 v[32:35], v[64:67], v[52:55], v[32:35]
	v_mfma_f32_16x16x32_f16 v[40:43], v[68:71], v[52:55], v[40:43]
	v_mfma_f32_16x16x32_f16 v[48:51], v[72:75], v[52:55], v[48:51]
	v_mfma_f32_16x16x32_f16 v[36:39], v[60:63], v[56:59], v[36:39]
	v_mfma_f32_16x16x32_f16 v[44:47], v[64:67], v[56:59], v[44:47]
	v_mfma_f32_16x16x32_f16 v[28:31], v[68:71], v[56:59], v[28:31]
	v_mfma_f32_16x16x32_f16 v[20:23], v[72:75], v[56:59], v[20:23]
	s_waitcnt lgkmcnt(0)
	v_mfma_f32_16x16x32_f16 v[24:27], v[84:87], v[76:79], v[24:27]
	ds_read_b128 v[52:55], v10 offset:32768
	ds_read_b128 v[56:59], v10 offset:34816
	v_mfma_f32_16x16x32_f16 v[32:35], v[88:91], v[76:79], v[32:35]
	v_mfma_f32_16x16x32_f16 v[40:43], v[92:95], v[76:79], v[40:43]
	ds_read_b128 v[60:63], v9 offset:49152
	ds_read_b128 v[64:67], v9 offset:51200
	v_mfma_f32_16x16x32_f16 v[48:51], v[96:99], v[76:79], v[48:51]
	v_mfma_f32_16x16x32_f16 v[36:39], v[84:87], v[80:83], v[36:39]
	ds_read_b128 v[68:71], v9 offset:53248
	ds_read_b128 v[72:75], v9 offset:55296
	v_mfma_f32_16x16x32_f16 v[44:47], v[88:91], v[80:83], v[44:47]
	v_mfma_f32_16x16x32_f16 v[28:31], v[92:95], v[80:83], v[28:31]
	v_mfma_f32_16x16x32_f16 v[20:23], v[96:99], v[80:83], v[20:23]
	s_mov_b64 s[20:21], 0x680
	s_mov_b32 m0, s16
	s_waitcnt vmcnt(4) lgkmcnt(0)
	s_barrier
	v_lshl_add_u64 v[76:77], v[4:5], 0, s[20:21]
	v_lshl_add_u64 v[78:79], v[6:7], 0, s[20:21]
	s_mov_b64 s[20:21], 0x20680
	global_load_lds_dwordx4 v[78:79], off
	v_lshl_add_u64 v[78:79], v[6:7], 0, s[20:21]
	s_mov_b32 m0, s13
	s_nop 0
	global_load_lds_dwordx4 v[78:79], off
	s_mov_b32 m0, s14
	s_nop 0
	global_load_lds_dwordx4 v[76:77], off
	v_lshl_add_u64 v[76:77], v[4:5], 0, s[20:21]
	s_mov_b32 m0, s15
	s_nop 0
	global_load_lds_dwordx4 v[76:77], off
	ds_read_b128 v[76:79], v12
	ds_read_b128 v[80:83], v13
	ds_read_b128 v[84:87], v14
	ds_read_b128 v[88:91], v15
	ds_read_b128 v[92:95], v16
	ds_read_b128 v[96:99], v17
	v_mfma_f32_16x16x32_f16 v[24:27], v[60:63], v[52:55], v[24:27]
	v_mfma_f32_16x16x32_f16 v[32:35], v[64:67], v[52:55], v[32:35]
	v_mfma_f32_16x16x32_f16 v[40:43], v[68:71], v[52:55], v[40:43]
	v_mfma_f32_16x16x32_f16 v[48:51], v[72:75], v[52:55], v[48:51]
	v_mfma_f32_16x16x32_f16 v[36:39], v[60:63], v[56:59], v[36:39]
	v_mfma_f32_16x16x32_f16 v[44:47], v[64:67], v[56:59], v[44:47]
	v_mfma_f32_16x16x32_f16 v[28:31], v[68:71], v[56:59], v[28:31]
	v_mfma_f32_16x16x32_f16 v[20:23], v[72:75], v[56:59], v[20:23]
	s_waitcnt lgkmcnt(0)
	v_mfma_f32_16x16x32_f16 v[24:27], v[84:87], v[76:79], v[24:27]
	ds_read_b128 v[52:55], v19
	ds_read_b128 v[56:59], v19 offset:2048
	v_mfma_f32_16x16x32_f16 v[32:35], v[88:91], v[76:79], v[32:35]
	v_mfma_f32_16x16x32_f16 v[40:43], v[92:95], v[76:79], v[40:43]
	ds_read_b128 v[60:63], v18 offset:16384
	ds_read_b128 v[64:67], v18 offset:18432
	v_mfma_f32_16x16x32_f16 v[48:51], v[96:99], v[76:79], v[48:51]
	v_mfma_f32_16x16x32_f16 v[36:39], v[84:87], v[80:83], v[36:39]
	ds_read_b128 v[68:71], v18 offset:20480
	ds_read_b128 v[72:75], v18 offset:22528
	v_mfma_f32_16x16x32_f16 v[44:47], v[88:91], v[80:83], v[44:47]
	v_mfma_f32_16x16x32_f16 v[28:31], v[92:95], v[80:83], v[28:31]
	v_mfma_f32_16x16x32_f16 v[20:23], v[96:99], v[80:83], v[20:23]
	s_mov_b64 s[14:15], 0x700
	s_mov_b32 m0, s18
	s_waitcnt vmcnt(4) lgkmcnt(0)
	s_barrier
	v_lshl_add_u64 v[76:77], v[4:5], 0, s[14:15]
	v_lshl_add_u64 v[78:79], v[6:7], 0, s[14:15]
	s_mov_b64 s[14:15], 0x20700
	global_load_lds_dwordx4 v[78:79], off
	v_lshl_add_u64 v[78:79], v[6:7], 0, s[14:15]
	s_mov_b32 m0, s17
	s_nop 0
	global_load_lds_dwordx4 v[78:79], off
	s_mov_b32 m0, s7
	s_nop 0
	global_load_lds_dwordx4 v[76:77], off
	v_lshl_add_u64 v[76:77], v[4:5], 0, s[14:15]
	s_mov_b32 m0, s12
	s_nop 0
	global_load_lds_dwordx4 v[76:77], off
	ds_read_b128 v[76:79], v11
	ds_read_b128 v[80:83], v11 offset:2048
	ds_read_b128 v[84:87], v2 offset:16384
	ds_read_b128 v[88:91], v2 offset:18432
	ds_read_b128 v[92:95], v2 offset:20480
	ds_read_b128 v[96:99], v2 offset:22528
	v_mfma_f32_16x16x32_f16 v[24:27], v[60:63], v[52:55], v[24:27]
	v_mfma_f32_16x16x32_f16 v[32:35], v[64:67], v[52:55], v[32:35]
	v_mfma_f32_16x16x32_f16 v[40:43], v[68:71], v[52:55], v[40:43]
	v_mfma_f32_16x16x32_f16 v[48:51], v[72:75], v[52:55], v[48:51]
	v_mfma_f32_16x16x32_f16 v[36:39], v[60:63], v[56:59], v[36:39]
	v_mfma_f32_16x16x32_f16 v[44:47], v[64:67], v[56:59], v[44:47]
	v_mfma_f32_16x16x32_f16 v[28:31], v[68:71], v[56:59], v[28:31]
	v_mfma_f32_16x16x32_f16 v[20:23], v[72:75], v[56:59], v[20:23]
	s_waitcnt lgkmcnt(0)
	v_mfma_f32_16x16x32_f16 v[24:27], v[84:87], v[76:79], v[24:27]
	ds_read_b128 v[52:55], v10
	ds_read_b128 v[56:59], v10 offset:2048
	v_mfma_f32_16x16x32_f16 v[32:35], v[88:91], v[76:79], v[32:35]
	v_mfma_f32_16x16x32_f16 v[40:43], v[92:95], v[76:79], v[40:43]
	ds_read_b128 v[60:63], v9 offset:16384
	ds_read_b128 v[64:67], v9 offset:18432
	v_mfma_f32_16x16x32_f16 v[48:51], v[96:99], v[76:79], v[48:51]
	v_mfma_f32_16x16x32_f16 v[36:39], v[84:87], v[80:83], v[36:39]
	ds_read_b128 v[68:71], v9 offset:20480
	ds_read_b128 v[72:75], v9 offset:22528
	v_mfma_f32_16x16x32_f16 v[44:47], v[88:91], v[80:83], v[44:47]
	v_mfma_f32_16x16x32_f16 v[28:31], v[92:95], v[80:83], v[28:31]
	v_mfma_f32_16x16x32_f16 v[20:23], v[96:99], v[80:83], v[20:23]
	s_mov_b32 m0, s6
	s_mov_b64 s[6:7], 0x780
	s_waitcnt vmcnt(4) lgkmcnt(0)
	s_barrier
	v_lshl_add_u64 v[76:77], v[4:5], 0, s[6:7]
	v_lshl_add_u64 v[78:79], v[6:7], 0, s[6:7]
	s_mov_b64 s[6:7], 0x20780
	global_load_lds_dwordx4 v[78:79], off
	v_lshl_add_u64 v[6:7], v[6:7], 0, s[6:7]
	s_mov_b32 m0, s3
	v_lshl_add_u64 v[4:5], v[4:5], 0, s[6:7]
	global_load_lds_dwordx4 v[6:7], off
	s_mov_b32 m0, s4
	s_nop 0
	global_load_lds_dwordx4 v[76:77], off
	s_mov_b32 m0, s5
	s_nop 0
	global_load_lds_dwordx4 v[4:5], off
	ds_read_b128 v[4:7], v11 offset:32768
	ds_read_b128 v[76:79], v11 offset:34816
	ds_read_b128 v[80:83], v2 offset:49152
	ds_read_b128 v[84:87], v2 offset:51200
	ds_read_b128 v[88:91], v2 offset:53248
	ds_read_b128 v[92:95], v2 offset:55296
	v_mfma_f32_16x16x32_f16 v[24:27], v[60:63], v[52:55], v[24:27]
	v_mfma_f32_16x16x32_f16 v[32:35], v[64:67], v[52:55], v[32:35]
	v_mfma_f32_16x16x32_f16 v[40:43], v[68:71], v[52:55], v[40:43]
	v_mfma_f32_16x16x32_f16 v[48:51], v[72:75], v[52:55], v[48:51]
	v_mfma_f32_16x16x32_f16 v[36:39], v[60:63], v[56:59], v[36:39]
	v_mfma_f32_16x16x32_f16 v[44:47], v[64:67], v[56:59], v[44:47]
	v_mfma_f32_16x16x32_f16 v[28:31], v[68:71], v[56:59], v[28:31]
	v_mfma_f32_16x16x32_f16 v[20:23], v[72:75], v[56:59], v[20:23]
	s_waitcnt lgkmcnt(0)
	v_mfma_f32_16x16x32_f16 v[24:27], v[80:83], v[4:7], v[24:27]
	v_mfma_f32_16x16x32_f16 v[32:35], v[84:87], v[4:7], v[32:35]
	v_mfma_f32_16x16x32_f16 v[40:43], v[88:91], v[4:7], v[40:43]
	v_mfma_f32_16x16x32_f16 v[4:7], v[92:95], v[4:7], v[48:51]
	s_nop 2
	ds_read_b128 v[48:51], v10 offset:32768
	ds_read_b128 v[52:55], v10 offset:34816
	ds_read_b128 v[56:59], v9 offset:49152
	ds_read_b128 v[60:63], v9 offset:51200
	ds_read_b128 v[64:67], v9 offset:53248
	ds_read_b128 v[68:71], v9 offset:55296
	v_mfma_f32_16x16x32_f16 v[36:39], v[80:83], v[76:79], v[36:39]
	v_mfma_f32_16x16x32_f16 v[44:47], v[84:87], v[76:79], v[44:47]
	v_mfma_f32_16x16x32_f16 v[28:31], v[88:91], v[76:79], v[28:31]
	v_mfma_f32_16x16x32_f16 v[20:23], v[92:95], v[76:79], v[20:23]
	s_waitcnt vmcnt(4) lgkmcnt(0)
	s_barrier
	ds_read_b128 v[72:75], v12
	ds_read_b128 v[76:79], v13
	ds_read_b128 v[80:83], v14
	ds_read_b128 v[12:15], v15
	ds_read_b128 v[84:87], v16
	ds_read_b128 v[88:91], v17
	v_mfma_f32_16x16x32_f16 v[24:27], v[56:59], v[48:51], v[24:27]
	v_mfma_f32_16x16x32_f16 v[32:35], v[60:63], v[48:51], v[32:35]
	v_mfma_f32_16x16x32_f16 v[40:43], v[64:67], v[48:51], v[40:43]
	v_mfma_f32_16x16x32_f16 v[4:7], v[68:71], v[48:51], v[4:7]
	v_mfma_f32_16x16x32_f16 v[36:39], v[56:59], v[52:55], v[36:39]
	v_mfma_f32_16x16x32_f16 v[44:47], v[60:63], v[52:55], v[44:47]
	v_mfma_f32_16x16x32_f16 v[28:31], v[64:67], v[52:55], v[28:31]
	v_mfma_f32_16x16x32_f16 v[20:23], v[68:71], v[52:55], v[20:23]
	s_waitcnt lgkmcnt(0)
	v_mfma_f32_16x16x32_f16 v[32:35], v[12:15], v[72:75], v[32:35]
	v_mfma_f32_16x16x32_f16 v[12:15], v[12:15], v[76:79], v[44:47]
	s_nop 2
	ds_read_b128 v[44:47], v19
	ds_read_b128 v[48:51], v19 offset:2048
	ds_read_b128 v[52:55], v18 offset:16384
	ds_read_b128 v[56:59], v18 offset:18432
	ds_read_b128 v[60:63], v18 offset:20480
	ds_read_b128 v[16:19], v18 offset:22528
	v_mfma_f32_16x16x32_f16 v[24:27], v[80:83], v[72:75], v[24:27]
	v_mfma_f32_16x16x32_f16 v[40:43], v[84:87], v[72:75], v[40:43]
	v_mfma_f32_16x16x32_f16 v[4:7], v[88:91], v[72:75], v[4:7]
	v_mfma_f32_16x16x32_f16 v[36:39], v[80:83], v[76:79], v[36:39]
	v_mfma_f32_16x16x32_f16 v[28:31], v[84:87], v[76:79], v[28:31]
	v_mfma_f32_16x16x32_f16 v[20:23], v[88:91], v[76:79], v[20:23]
	s_waitcnt vmcnt(0) lgkmcnt(0)
	s_barrier
	ds_read_b128 v[64:67], v11
	ds_read_b128 v[68:71], v11 offset:2048
	ds_read_b128 v[72:75], v2 offset:16384
	ds_read_b128 v[76:79], v2 offset:18432
	ds_read_b128 v[80:83], v2 offset:20480
	ds_read_b128 v[84:87], v2 offset:22528
	v_mfma_f32_16x16x32_f16 v[24:27], v[52:55], v[44:47], v[24:27]
	v_mfma_f32_16x16x32_f16 v[32:35], v[56:59], v[44:47], v[32:35]
	v_mfma_f32_16x16x32_f16 v[40:43], v[60:63], v[44:47], v[40:43]
	v_mfma_f32_16x16x32_f16 v[4:7], v[16:19], v[44:47], v[4:7]
	v_mfma_f32_16x16x32_f16 v[36:39], v[52:55], v[48:51], v[36:39]
	v_mfma_f32_16x16x32_f16 v[12:15], v[56:59], v[48:51], v[12:15]
	v_mfma_f32_16x16x32_f16 v[28:31], v[60:63], v[48:51], v[28:31]
	v_mfma_f32_16x16x32_f16 v[16:19], v[16:19], v[48:51], v[20:23]
	s_waitcnt lgkmcnt(3)
	v_mfma_f32_16x16x32_f16 v[20:23], v[72:75], v[64:67], v[24:27]
	s_waitcnt lgkmcnt(2)
	v_mfma_f32_16x16x32_f16 v[24:27], v[76:79], v[64:67], v[32:35]
	s_waitcnt lgkmcnt(1)
	v_mfma_f32_16x16x32_f16 v[32:35], v[80:83], v[64:67], v[40:43]
	s_nop 2
	ds_read_b128 v[40:43], v10
	ds_read_b128 v[44:47], v10 offset:2048
	ds_read_b128 v[48:51], v9 offset:16384
	ds_read_b128 v[52:55], v9 offset:18432
	ds_read_b128 v[56:59], v9 offset:20480
	ds_read_b128 v[60:63], v9 offset:22528
	s_waitcnt lgkmcnt(6)
	v_mfma_f32_16x16x32_f16 v[4:7], v[84:87], v[64:67], v[4:7]
	v_mfma_f32_16x16x32_f16 v[36:39], v[72:75], v[68:71], v[36:39]
	v_mfma_f32_16x16x32_f16 v[12:15], v[76:79], v[68:71], v[12:15]
	v_mfma_f32_16x16x32_f16 v[28:31], v[80:83], v[68:71], v[28:31]
	v_mfma_f32_16x16x32_f16 v[16:19], v[84:87], v[68:71], v[16:19]
	s_waitcnt vmcnt(0) lgkmcnt(0)
	s_barrier
	v_and_b32_e32 v2, 64, v0
	v_lshrrev_b32_e32 v9, 6, v0
	v_mfma_f32_16x16x32_f16 v[20:23], v[48:51], v[40:43], v[20:23]
	v_mfma_f32_16x16x32_f16 v[24:27], v[52:55], v[40:43], v[24:27]
	v_mfma_f32_16x16x32_f16 v[32:35], v[56:59], v[40:43], v[32:35]
	v_mfma_f32_16x16x32_f16 v[4:7], v[60:63], v[40:43], v[4:7]
	v_mfma_f32_16x16x32_f16 v[36:39], v[48:51], v[44:47], v[36:39]
	v_mfma_f32_16x16x32_f16 v[10:13], v[52:55], v[44:47], v[12:15]
	v_mfma_f32_16x16x32_f16 v[28:31], v[56:59], v[44:47], v[28:31]
	v_mfma_f32_16x16x32_f16 v[14:17], v[60:63], v[44:47], v[16:19]
	s_movk_i32 s3, 0x2200
	v_mad_u32_u24 v9, v9, s3, 0
	s_nop 0
	v_and_b32_e32 v18, 48, v0
	v_mul_u32_u24_e32 v19, 0x110, v8
	v_add3_u32 v18, v9, v18, v19
	s_barrier
	ds_write_b128 v18, v[20:23]
	ds_write_b128 v18, v[24:27] offset:64
	ds_write_b128 v18, v[32:35] offset:128
	ds_write_b128 v18, v[4:7] offset:192
	ds_write_b128 v18, v[36:39] offset:4352
	ds_write_b128 v18, v[10:13] offset:4416
	ds_write_b128 v18, v[28:31] offset:4480
	ds_write_b128 v18, v[14:17] offset:4544
	v_lshlrev_b32_e32 v4, 2, v8
	v_or3_b32 v2, v4, v2, s2
	v_lshlrev_b64 v[10:11], 2, v[2:3]
	s_waitcnt lgkmcnt(0)
	v_lshl_add_u64 v[2:3], s[10:11], 0, v[10:11]
	global_load_dwordx4 v[2:5], v[2:3], off
	v_bfe_u32 v0, v0, 4, 2
	v_lshlrev_b32_e32 v6, 4, v8
	v_mul_u32_u24_e32 v7, 0x110, v0
	v_add3_u32 v13, v9, v6, v7
	ds_read_b128 v[6:9], v13
	v_or3_b32 v12, s1, v1, v0
	v_mad_i64_i32 v[0:1], s[2:3], v12, s0, 0
	v_lshl_add_u64 v[0:1], v[0:1], 2, s[8:9]
	v_lshl_add_u64 v[0:1], v[0:1], 0, v[10:11]
	v_or_b32_e32 v14, 4, v12
	v_or_b32_e32 v15, 8, v12
	v_or_b32_e32 v16, 12, v12
	v_or_b32_e32 v17, 16, v12
	v_or_b32_e32 v18, 20, v12
	v_or_b32_e32 v19, 24, v12
	v_or_b32_e32 v12, 28, v12
	s_waitcnt vmcnt(0) lgkmcnt(0)
	v_pk_add_f32 v[8:9], v[4:5], v[8:9]
	v_pk_add_f32 v[6:7], v[2:3], v[6:7]
	s_nop 0
	global_store_dwordx4 v[0:1], v[6:9], off sc1
	s_nop 1
	ds_read_b128 v[6:9], v13 offset:1088
	v_mad_i64_i32 v[0:1], s[2:3], v14, s0, 0
	v_lshl_add_u64 v[0:1], v[0:1], 2, s[8:9]
	v_lshl_add_u64 v[0:1], v[0:1], 0, v[10:11]
	s_waitcnt lgkmcnt(0)
	v_pk_add_f32 v[8:9], v[4:5], v[8:9]
	v_pk_add_f32 v[6:7], v[2:3], v[6:7]
	s_nop 0
	global_store_dwordx4 v[0:1], v[6:9], off sc1
	s_nop 1
	ds_read_b128 v[6:9], v13 offset:2176
	v_mad_i64_i32 v[0:1], s[2:3], v15, s0, 0
	v_lshl_add_u64 v[0:1], v[0:1], 2, s[8:9]
	v_lshl_add_u64 v[0:1], v[0:1], 0, v[10:11]
	s_waitcnt lgkmcnt(0)
	v_pk_add_f32 v[8:9], v[4:5], v[8:9]
	v_pk_add_f32 v[6:7], v[2:3], v[6:7]
	s_nop 0
	global_store_dwordx4 v[0:1], v[6:9], off sc1
	s_nop 1
	ds_read_b128 v[6:9], v13 offset:3264
	v_mad_i64_i32 v[0:1], s[2:3], v16, s0, 0
	v_lshl_add_u64 v[0:1], v[0:1], 2, s[8:9]
	v_lshl_add_u64 v[0:1], v[0:1], 0, v[10:11]
	s_waitcnt lgkmcnt(0)
	v_pk_add_f32 v[8:9], v[4:5], v[8:9]
	v_pk_add_f32 v[6:7], v[2:3], v[6:7]
	s_nop 0
	global_store_dwordx4 v[0:1], v[6:9], off sc1
	s_nop 1
	ds_read_b128 v[6:9], v13 offset:4352
	v_mad_i64_i32 v[0:1], s[2:3], v17, s0, 0
	v_lshl_add_u64 v[0:1], v[0:1], 2, s[8:9]
	v_lshl_add_u64 v[0:1], v[0:1], 0, v[10:11]
	s_waitcnt lgkmcnt(0)
	v_pk_add_f32 v[8:9], v[4:5], v[8:9]
	v_pk_add_f32 v[6:7], v[2:3], v[6:7]
	s_nop 0
	global_store_dwordx4 v[0:1], v[6:9], off sc1
	s_nop 1
	ds_read_b128 v[6:9], v13 offset:5440
	v_mad_i64_i32 v[0:1], s[2:3], v18, s0, 0
	v_lshl_add_u64 v[0:1], v[0:1], 2, s[8:9]
	v_lshl_add_u64 v[0:1], v[0:1], 0, v[10:11]
	s_waitcnt lgkmcnt(0)
	v_pk_add_f32 v[8:9], v[4:5], v[8:9]
	v_pk_add_f32 v[6:7], v[2:3], v[6:7]
	s_nop 0
	global_store_dwordx4 v[0:1], v[6:9], off sc1
	s_nop 1
	ds_read_b128 v[6:9], v13 offset:6528
	v_mad_i64_i32 v[0:1], s[2:3], v19, s0, 0
	v_lshl_add_u64 v[0:1], v[0:1], 2, s[8:9]
	v_lshl_add_u64 v[0:1], v[0:1], 0, v[10:11]
	s_waitcnt lgkmcnt(0)
	v_pk_add_f32 v[8:9], v[4:5], v[8:9]
	v_pk_add_f32 v[6:7], v[2:3], v[6:7]
	s_nop 0
	global_store_dwordx4 v[0:1], v[6:9], off sc1
	s_nop 1
	ds_read_b128 v[6:9], v13 offset:7616
	v_mad_i64_i32 v[0:1], s[0:1], v12, s0, 0
	v_lshl_add_u64 v[0:1], v[0:1], 2, s[8:9]
	v_lshl_add_u64 v[0:1], v[0:1], 0, v[10:11]
	s_waitcnt lgkmcnt(0)
	v_pk_add_f32 v[4:5], v[4:5], v[8:9]
	v_pk_add_f32 v[2:3], v[2:3], v[6:7]
	s_nop 0
	global_store_dwordx4 v[0:1], v[2:5], off sc1
	s_nop 1
	s_endpgm
